# speedup vs baseline: 1.0069x; 1.0036x over previous
.LBB3_61:
	s_or_b64 exec, exec, s[4:5]
	s_movk_i32 s5, 0x2b0
	v_mov_b32_e32 v5, 0x15000
	v_mad_u32_u24 v206, v0, s5, v5
	v_mov_b32_e32 v5, 0x3c00
	v_cmp_eq_u32_e32 vcc, 0, v55
	s_movk_i32 s4, 0xf0
	v_mul_u32_u24_e32 v3, 56, v55
	v_cndmask_b32_e32 v208, 0, v5, vcc
	v_lshlrev_b32_e32 v5, 3, v204
	v_lshl_or_b32 v5, v195, 8, v5
	v_add_u32_e32 v209, 0x26a80, v5
	v_mov_b32_e32 v5, 0x23800
	v_mov_b32_e32 v2, 0x1fc00
	v_mad_u32_u24 v4, v204, s5, v3
	s_mov_b32 s8, 0x15000
	v_mad_u32_u24 v207, v204, s4, v5
	v_lshlrev_b32_e32 v5, 3, v205
	v_lshlrev_b32_e32 v194, 4, v205
	v_mad_u32_u24 v2, v204, s4, v2
	v_add3_u32 v210, v207, v3, v5
	v_add3_u32 v212, v4, v194, s8
	s_movk_i32 s4, 0x64
	v_mov_b32_e32 v4, 0x25600
	v_mad_u32_u24 v214, v0, s4, v4
	v_add_u32_e32 v0, 48, v210
	v_cmp_gt_u32_e64 s[4:5], 32, v1
	v_add_u32_e32 v211, v2, v194
	v_add3_u32 v217, v2, v3, v5
	v_cndmask_b32_e64 v218, v209, v0, s[4:5]
	v_mul_u32_u24_e32 v0, 0x1c0, v195
	v_or_b32_e32 v0, v0, v1
	v_lshlrev_b32_e32 v0, 4, v0
	v_mov_b32_e32 v1, 0
	v_add_u32_e32 v2, 0x1000, v0
	v_mov_b32_e32 v3, v1
	v_lshl_add_u64 v[196:197], s[0:1], 0, v[0:1]
	v_lshl_add_u64 v[198:199], s[0:1], 0, v[2:3]
	v_add_u32_e32 v2, 0x1400, v0
	v_add_u32_e32 v0, 0x1800, v0
	v_add_u32_e32 v213, 0x26280, v50
	v_lshl_add_u32 v215, v54, 4, v50
	v_lshl_add_u64 v[200:201], s[0:1], 0, v[2:3]
	v_lshl_add_u64 v[202:203], s[0:1], 0, v[0:1]
	v_mov_b32_e32 v0, v1
	v_mov_b32_e32 v2, v1
	v_mov_b32_e32 v4, v1
	v_mov_b32_e32 v5, v1
	v_mov_b32_e32 v6, v1
	v_mov_b32_e32 v7, v1
	v_mov_b32_e32 v8, v1
	v_mov_b32_e32 v9, v1
	v_mov_b32_e32 v10, v1
	v_mov_b32_e32 v11, v1
	v_mov_b32_e32 v12, v1
	v_mov_b64_e32 v[80:81], v[14:15]
	v_mov_b64_e32 v[64:65], v[14:15]
	v_mov_b64_e32 v[48:49], v[14:15]
	s_mov_b32 s14, 0
	v_add_u32_e32 v216, v207, v194
	s_mov_b32 s15, 0x5040100
	s_movk_i32 s18, 0x2a0
	v_mov_b64_e32 v[78:79], v[12:13]
	v_mov_b64_e32 v[76:77], v[10:11]
	v_mov_b64_e32 v[74:75], v[8:9]
	v_mov_b64_e32 v[72:73], v[6:7]
	v_mov_b64_e32 v[70:71], v[4:5]
	v_mov_b64_e32 v[68:69], v[2:3]
	v_mov_b64_e32 v[66:67], v[0:1]
	v_mov_b64_e32 v[62:63], v[12:13]
	v_mov_b64_e32 v[60:61], v[10:11]
	v_mov_b64_e32 v[58:59], v[8:9]
	v_mov_b64_e32 v[56:57], v[6:7]
	v_mov_b64_e32 v[54:55], v[4:5]
	v_mov_b64_e32 v[52:53], v[2:3]
	v_mov_b64_e32 v[50:51], v[0:1]
	v_mov_b64_e32 v[46:47], v[12:13]
	v_mov_b64_e32 v[44:45], v[10:11]
	v_mov_b64_e32 v[42:43], v[8:9]
	v_mov_b64_e32 v[40:41], v[6:7]
	v_mov_b64_e32 v[38:39], v[4:5]
	v_mov_b64_e32 v[36:37], v[2:3]
	v_mov_b64_e32 v[34:35], v[0:1]
	v_mov_b32_e32 v13, v1
	v_mov_b32_e32 v14, v1
	v_mov_b32_e32 v15, v1
	v_mov_b32_e32 v16, v1
	v_mov_b32_e32 v17, v1
	v_mov_b32_e32 v18, v1
	v_mov_b32_e32 v19, v1
	v_mov_b32_e32 v20, v1
	v_mov_b32_e32 v21, v1
	v_mov_b32_e32 v22, v1
	v_mov_b32_e32 v23, v1
	v_mov_b32_e32 v24, v1
	v_mov_b32_e32 v25, v1
	v_mov_b32_e32 v26, v1
	v_mov_b32_e32 v27, v1
	v_mov_b32_e32 v28, v1
	v_mov_b32_e32 v29, v1
	v_mov_b32_e32 v30, v1
	s_cmp_eq_u32 s47, 2
	s_cbranch_scc1 .Lgru_restore
	s_cmp_lt_u32 s72, 0x100
	s_cbranch_scc1 .Lapf_skip_a
	ds_read_b128 v[232:235], v215
	ds_read_b128 v[236:239], v215 offset:7168
	ds_read_b128 v[240:243], v215 offset:14336
	ds_read_b128 v[244:247], v215 offset:1024
	ds_read_b128 v[200:203], v215 offset:8192
.Lapf_skip_a:
	s_waitcnt lgkmcnt(0)
	s_barrier
	s_branch .LBB3_63

.LBB3_63:
	s_cmp_eq_u32 s14, s50
	s_cbranch_scc1 .Lgru_dump
	s_and_saveexec_b64 s[0:1], s[6:7]
	s_xor_b64 s[0:1], exec, s[0:1]
	s_cbranch_execz .LBB3_66
	s_and_b32 s21, s14, 1
	s_mulk_i32 s21, 0x1e00
	v_add_u32_e32 v231, s21, v211
	ds_read_b128 v[166:169], v231
	ds_read_b128 v[170:173], v231 offset:32
	ds_read_b128 v[174:177], v231 offset:64
	ds_read_b128 v[178:181], v231 offset:96
	ds_read_b128 v[182:185], v231 offset:128
	ds_read_b128 v[186:189], v231 offset:160
	ds_read_b128 v[196:199], v231 offset:192
	s_cmp_lt_u32 s14, 2
	s_cbranch_scc1 .LBB3_66
	v_exp_f32_e32 v0, v2
	v_exp_f32_e32 v2, v3
	v_exp_f32_e32 v3, v4
	v_exp_f32_e32 v4, v5
	v_exp_f32_e32 v5, v6
	v_exp_f32_e32 v6, v7
	v_exp_f32_e32 v7, v8
	v_exp_f32_e32 v8, v9
	v_exp_f32_e32 v9, v10
	v_exp_f32_e32 v10, v11
	v_exp_f32_e32 v11, v12
	v_exp_f32_e32 v12, v13
	v_exp_f32_e32 v13, v14
	v_add_f32_e32 v0, 1.0, v0
	v_exp_f32_e32 v14, v18
	v_exp_f32_e32 v18, v19
	v_exp_f32_e32 v19, v20
	v_exp_f32_e32 v20, v21
	v_exp_f32_e32 v21, v22
	v_exp_f32_e32 v22, v23
	v_exp_f32_e32 v23, v24
	v_exp_f32_e32 v24, v25
	v_exp_f32_e32 v25, v26
	v_exp_f32_e32 v26, v27
	v_exp_f32_e32 v27, v28
	v_exp_f32_e32 v28, v29
	v_exp_f32_e32 v29, v30
	v_add_f32_e32 v30, 1.0, v2
	v_add_f32_e32 v65, 1.0, v11
	v_rcp_f32_e32 v2, v0
	v_add_f32_e32 v79, 1.0, v12
	v_rcp_f32_e32 v12, v65
	v_add_f32_e32 v31, 1.0, v3
	v_rcp_f32_e32 v3, v30
	v_add_f32_e32 v47, 1.0, v6
	v_add_f32_e32 v80, 1.0, v13
	v_rcp_f32_e32 v13, v79
	v_add_f32_e32 v32, 1.0, v4
	v_add_f32_e32 v48, 1.0, v7
	v_rcp_f32_e32 v4, v31
	v_rcp_f32_e32 v7, v47
	v_fma_f32 v0, v2, v34, v66
	v_add_f32_e32 v81, 1.0, v14
	v_rcp_f32_e32 v14, v80
	v_fma_f32 v66, v12, v44, v76
	v_exp_f32_e32 v0, v0
	v_add_f32_e32 v33, 1.0, v5
	v_add_f32_e32 v49, 1.0, v8
	v_rcp_f32_e32 v5, v32
	v_rcp_f32_e32 v8, v48
	v_fma_f32 v31, v3, v35, v67
	v_exp_f32_e32 v66, v66
	v_fma_f32 v67, v13, v45, v77
	v_exp_f32_e32 v31, v31
	v_rcp_f32_e32 v6, v33
	v_fma_f32 v32, v4, v36, v68
	v_fma_f32 v48, v7, v39, v71
	v_exp_f32_e32 v67, v67
	v_fma_f32 v68, v14, v46, v78
	v_exp_f32_e32 v32, v32
	v_exp_f32_e32 v48, v48
	v_add_f32_e32 v0, 1.0, v0
	v_add_f32_e32 v63, 1.0, v9
	v_rcp_f32_e32 v9, v49
	v_fma_f32 v33, v5, v37, v69
	v_fma_f32 v49, v8, v40, v72
	v_exp_f32_e32 v68, v68
	v_add_f32_e32 v76, 1.0, v66
	v_rcp_f32_e32 v66, v0
	v_exp_f32_e32 v33, v33
	v_exp_f32_e32 v49, v49
	v_add_f32_e32 v31, 1.0, v31
	v_fma_f32 v47, v6, v38, v70
	v_add_f32_e32 v77, 1.0, v67
	v_rcp_f32_e32 v67, v31
	v_add_f32_e32 v219, 1.0, v18
	v_rcp_f32_e32 v18, v81
	v_exp_f32_e32 v47, v47
	v_add_f32_e32 v32, 1.0, v32
	v_add_f32_e32 v48, 1.0, v48
	v_add_f32_e32 v78, 1.0, v68
	v_rcp_f32_e32 v68, v32
	v_rcp_f32_e32 v71, v48
	v_fma_f32 v66, v66, -2.0, 1.0
	v_add_f32_e32 v220, 1.0, v19
	v_rcp_f32_e32 v19, v219
	v_add_f32_e32 v33, 1.0, v33
	v_add_f32_e32 v49, 1.0, v49
	v_add_f32_e32 v64, 1.0, v10
	v_sub_f32_e32 v0, v50, v66
	v_rcp_f32_e32 v10, v63
	v_rcp_f32_e32 v69, v33
	v_rcp_f32_e32 v72, v49
	v_fma_f32 v67, v67, -2.0, 1.0
	v_add_f32_e32 v221, 1.0, v20
	v_rcp_f32_e32 v20, v220
	v_add_f32_e32 v47, 1.0, v47
	v_fma_f32 v50, v18, v0, v66
	v_rcp_f32_e32 v11, v64
	v_sub_f32_e32 v0, v51, v67
	v_fma_f32 v63, v9, v41, v73
	v_rcp_f32_e32 v70, v47
	v_fma_f32 v68, v68, -2.0, 1.0
	v_add_f32_e32 v222, 1.0, v21
	v_rcp_f32_e32 v21, v221
	v_exp_f32_e32 v63, v63
	v_fma_f32 v51, v19, v0, v67
	v_fma_f32 v64, v10, v42, v74
	v_sub_f32_e32 v0, v52, v68
	v_fma_f32 v69, v69, -2.0, 1.0
	v_add_f32_e32 v223, 1.0, v22
	v_rcp_f32_e32 v22, v222
	v_exp_f32_e32 v64, v64
	v_fma_f32 v52, v20, v0, v68
	v_fma_f32 v65, v11, v43, v75
	v_sub_f32_e32 v0, v53, v69
	v_fma_f32 v70, v70, -2.0, 1.0
	v_add_f32_e32 v224, 1.0, v23
	v_rcp_f32_e32 v23, v223
	v_exp_f32_e32 v65, v65
	v_add_f32_e32 v63, 1.0, v63
	v_fma_f32 v53, v21, v0, v69
	v_rcp_f32_e32 v73, v63
	v_sub_f32_e32 v0, v54, v70
	v_fma_f32 v71, v71, -2.0, 1.0
	v_add_f32_e32 v225, 1.0, v24
	v_rcp_f32_e32 v24, v224
	v_add_f32_e32 v64, 1.0, v64
	v_fma_f32 v54, v22, v0, v70
	v_rcp_f32_e32 v74, v64
	v_sub_f32_e32 v0, v55, v71
	v_fma_f32 v72, v72, -2.0, 1.0
	v_add_f32_e32 v226, 1.0, v25
	v_rcp_f32_e32 v25, v225
	v_add_f32_e32 v65, 1.0, v65
	v_fma_f32 v55, v23, v0, v71
	v_rcp_f32_e32 v75, v65
	v_sub_f32_e32 v0, v56, v72
	v_fma_f32 v73, v73, -2.0, 1.0
	v_add_f32_e32 v227, 1.0, v26
	v_rcp_f32_e32 v26, v226
	v_fma_f32 v56, v24, v0, v72
	v_rcp_f32_e32 v76, v76
	v_sub_f32_e32 v0, v57, v73
	v_fma_f32 v74, v74, -2.0, 1.0
	v_add_f32_e32 v228, 1.0, v27
	v_rcp_f32_e32 v27, v227
	v_fma_f32 v57, v25, v0, v73
	v_rcp_f32_e32 v77, v77
	v_sub_f32_e32 v0, v58, v74
	v_fma_f32 v75, v75, -2.0, 1.0
	v_add_f32_e32 v229, 1.0, v28
	v_rcp_f32_e32 v28, v228
	v_fma_f32 v58, v26, v0, v74
	v_rcp_f32_e32 v78, v78
	v_sub_f32_e32 v0, v59, v75
	v_fma_f32 v76, v76, -2.0, 1.0
	v_add_f32_e32 v230, 1.0, v29
	v_rcp_f32_e32 v29, v229
	v_fma_f32 v59, v27, v0, v75
	v_rcp_f32_e32 v30, v230
	v_sub_f32_e32 v0, v60, v76
	v_fma_f32 v77, v77, -2.0, 1.0
	v_fma_f32 v60, v28, v0, v76
	v_fma_f32 v78, v78, -2.0, 1.0
	v_sub_f32_e32 v0, v61, v77
	s_nop 0
	v_fma_f32 v61, v29, v0, v77
	v_sub_f32_e32 v0, v62, v78
	s_nop 0
	v_fma_f32 v62, v30, v0, v78
	v_cvt_pk_f16_f32 v33, v52, v53
	v_cvt_f16_f32_e32 v0, v62
	v_cvt_pk_f16_f32 v32, v50, v51
	v_cvt_pk_f16_f32 v49, v56, v57
	v_cvt_pk_f16_f32 v48, v54, v55
	ds_write2_b64 v210, v[32:33], v[48:49] offset1:2
	v_cvt_pk_f16_f32 v33, v60, v61
	v_cvt_pk_f16_f32 v32, v58, v59
	v_perm_b32 v0, v208, v0, s15
	ds_write_b64 v210, v[32:33] offset:32
	ds_write_b64 v218, v[0:1]

.LBB3_78:
	s_andn2_b64 vcc, exec, s[8:9]
	s_cbranch_vccnz .LBB3_80
	s_setprio 1
	ds_read_b128 v[220:223], v215 offset:15360
	v_mfma_f32_32x32x16_f16 v[2:17], v[232:235], v[166:169], 0
	v_mfma_f32_32x32x16_f16 v[18:33], v[236:239], v[166:169], 0
	ds_read_b128 v[232:235], v215 offset:2048
	v_mfma_f32_32x32x16_f16 v[66:81], v[240:243], v[166:169], 0
	ds_read_b128 v[236:239], v215 offset:9216
	v_mfma_f32_32x32x16_f16 v[2:17], v[244:247], v[170:173], v[2:17]
	ds_read_b128 v[240:243], v215 offset:16384
	v_mfma_f32_32x32x16_f16 v[18:33], v[200:203], v[170:173], v[18:33]
	ds_read_b128 v[244:247], v215 offset:3072
	ds_read_b128 v[166:169], v216
	s_waitcnt lgkmcnt(5)
	v_mfma_f32_32x32x16_f16 v[66:81], v[220:223], v[170:173], v[66:81]
	ds_read_b128 v[200:203], v215 offset:10240
	s_waitcnt lgkmcnt(5)
	v_mfma_f32_32x32x16_f16 v[2:17], v[232:235], v[174:177], v[2:17]
	ds_read_b128 v[220:223], v215 offset:17408
	s_waitcnt lgkmcnt(5)
	v_mfma_f32_32x32x16_f16 v[18:33], v[236:239], v[174:177], v[18:33]
	ds_read_b128 v[232:235], v215 offset:4096
	ds_read_b128 v[170:173], v216 offset:32
	s_waitcnt lgkmcnt(6)
	v_mfma_f32_32x32x16_f16 v[66:81], v[240:243], v[174:177], v[66:81]
	ds_read_b128 v[236:239], v215 offset:11264
	s_waitcnt lgkmcnt(6)
	v_mfma_f32_32x32x16_f16 v[2:17], v[244:247], v[178:181], v[2:17]
	ds_read_b128 v[240:243], v215 offset:18432
	s_waitcnt lgkmcnt(5)
	v_mfma_f32_32x32x16_f16 v[18:33], v[200:203], v[178:181], v[18:33]
	ds_read_b128 v[244:247], v215 offset:5120
	ds_read_b128 v[174:177], v216 offset:64
	s_waitcnt lgkmcnt(6)
	v_mfma_f32_32x32x16_f16 v[66:81], v[220:223], v[178:181], v[66:81]
	ds_read_b128 v[200:203], v215 offset:12288
	s_waitcnt lgkmcnt(6)
	v_mfma_f32_32x32x16_f16 v[2:17], v[232:235], v[182:185], v[2:17]
	ds_read_b128 v[220:223], v215 offset:19456
	s_waitcnt lgkmcnt(5)
	v_mfma_f32_32x32x16_f16 v[18:33], v[236:239], v[182:185], v[18:33]
	ds_read_b128 v[232:235], v215 offset:6144
	ds_read_b128 v[178:181], v216 offset:96
	s_waitcnt lgkmcnt(6)
	v_mfma_f32_32x32x16_f16 v[66:81], v[240:243], v[182:185], v[66:81]
	ds_read_b128 v[236:239], v215 offset:13312
	s_waitcnt lgkmcnt(6)
	v_mfma_f32_32x32x16_f16 v[2:17], v[244:247], v[186:189], v[2:17]
	ds_read_b128 v[240:243], v215 offset:20480
	s_waitcnt lgkmcnt(5)
	v_mfma_f32_32x32x16_f16 v[18:33], v[200:203], v[186:189], v[18:33]
	ds_read_b128 v[182:185], v216 offset:128
	s_waitcnt lgkmcnt(5)
	v_mfma_f32_32x32x16_f16 v[66:81], v[220:223], v[186:189], v[66:81]
	s_waitcnt lgkmcnt(4)
	v_mfma_f32_32x32x16_f16 v[2:17], v[232:235], v[196:199], v[2:17]
	s_waitcnt lgkmcnt(2)
	v_mfma_f32_32x32x16_f16 v[18:33], v[236:239], v[196:199], v[18:33]
	ds_read_b128 v[186:189], v216 offset:160
	s_waitcnt lgkmcnt(2)
	v_mfma_f32_32x32x16_f16 v[66:81], v[240:243], v[196:199], v[66:81]
	v_mfma_f32_32x32x16_f16 v[2:17], v[82:85], v[166:169], v[2:17]
	v_mfma_f32_32x32x16_f16 v[18:33], v[130:133], v[166:169], v[18:33]
	ds_read_b128 v[196:199], v216 offset:192
	v_mfma_f32_32x32x16_f16 v[34:49], v[138:141], v[166:169], 0
	v_mfma_f32_32x32x16_f16 v[2:17], v[86:89], v[170:173], v[2:17]
	ds_read_b128 v[232:235], v215
	v_mfma_f32_32x32x16_f16 v[18:33], v[110:113], v[170:173], v[18:33]
	ds_read_b128 v[236:239], v215 offset:7168
	v_mfma_f32_32x32x16_f16 v[34:49], v[142:145], v[170:173], v[34:49]
	ds_read_b128 v[240:243], v215 offset:14336
	v_mfma_f32_32x32x16_f16 v[2:17], v[90:93], v[174:177], v[2:17]
	ds_read_b128 v[244:247], v215 offset:1024
	v_mfma_f32_32x32x16_f16 v[18:33], v[114:117], v[174:177], v[18:33]
	ds_read_b128 v[200:203], v215 offset:8192
	v_mfma_f32_32x32x16_f16 v[34:49], v[146:149], v[174:177], v[34:49]
	v_mfma_f32_32x32x16_f16 v[2:17], v[94:97], v[178:181], v[2:17]
	v_mfma_f32_32x32x16_f16 v[18:33], v[118:121], v[178:181], v[18:33]
	v_mfma_f32_32x32x16_f16 v[34:49], v[150:153], v[178:181], v[34:49]
	s_waitcnt lgkmcnt(7)
	v_mfma_f32_32x32x16_f16 v[2:17], v[106:109], v[182:185], v[2:17]
	v_mfma_f32_32x32x16_f16 v[18:33], v[122:125], v[182:185], v[18:33]
	v_mfma_f32_32x32x16_f16 v[34:49], v[154:157], v[182:185], v[34:49]
	s_waitcnt lgkmcnt(6)
	v_mfma_f32_32x32x16_f16 v[2:17], v[98:101], v[186:189], v[2:17]
	v_mfma_f32_32x32x16_f16 v[18:33], v[126:129], v[186:189], v[18:33]
	v_mfma_f32_32x32x16_f16 v[34:49], v[158:161], v[186:189], v[34:49]
	s_waitcnt lgkmcnt(5)
	v_mfma_f32_32x32x16_f16 v[2:17], v[102:105], v[196:199], v[2:17]
	v_mfma_f32_32x32x16_f16 v[18:33], v[134:137], v[196:199], v[18:33]
	v_mfma_f32_32x32x16_f16 v[34:49], v[162:165], v[196:199], v[34:49]
	s_setprio 0

.Lgru_rs_r3:
	v_add_u32_e32 v220, 0x400, v248
	v_min_u32_e32 v220, 0x59f, v220
	v_lshlrev_b32_e32 v220, 4, v220
	v_add_u32_e32 v221, 0x18000, v219
	v_add_u32_e32 v222, 0x1a000, v219
	v_add_u32_e32 v223, 0x18000, v220
	global_load_dwordx4 v[224:227], v221, s[58:59] sc0 sc1
	global_load_dwordx4 v[228:231], v222, s[58:59] sc0 sc1
	global_load_dwordx4 v[232:235], v223, s[58:59] sc0 sc1
	v_add_u32_e32 v221, 0x1fc00, v219
	v_add_u32_e32 v222, 0x1fc00, v220
	s_waitcnt vmcnt(2)
	ds_write_b128 v221, v[224:227]
	s_waitcnt vmcnt(1)
	ds_write_b128 v221, v[228:231] offset:8192
	s_waitcnt vmcnt(0)
	ds_write_b128 v222, v[232:235]
	s_movk_i32 s14, 16
	s_cmp_lt_u32 s72, 0x100
	s_cbranch_scc1 .Lapf_skip_b
	ds_read_b128 v[232:235], v215
	ds_read_b128 v[236:239], v215 offset:7168
	ds_read_b128 v[240:243], v215 offset:14336
	ds_read_b128 v[244:247], v215 offset:1024
	ds_read_b128 v[200:203], v215 offset:8192
